# in-proj K-loop: LDS-DMA stage instructions issued inside the following MFMA block, counted vmcnt re-derived
# baseline (speedup 1.0000x reference)
.LBB0_258:
	ds_read_b128 v[218:221], v214 offset:16384
	ds_read_b128 v[222:225], v214 offset:17408
	ds_read_b128 v[226:229], v215 offset:16384
	ds_read_b128 v[230:233], v215 offset:17408
	ds_read_b128 v[234:237], v216 offset:16384
	ds_read_b128 v[238:241], v216 offset:17408
	ds_read_b128 v[242:245], v217 offset:16384
	ds_read_b128 v[246:249], v217 offset:17408
	s_waitcnt vmcnt(2)
	s_waitcnt lgkmcnt(0)
	s_barrier
	s_setprio 1
	s_waitcnt lgkmcnt(0)
	v_mfma_scale_f32_16x16x128_f8f6f4 v[144:147], v[20:27], v[218:225], v[144:147], v186, v185 op_sel_hi:[0,0,0]
	v_mfma_scale_f32_16x16x128_f8f6f4 v[140:143], v[28:35], v[218:225], v[140:143], v186, v185 op_sel_hi:[0,0,0]
	s_lshl_b64 s[2:3], s[82:83], 7
	s_add_u32 s26, s4, s2
	v_mov_b32_e32 v2, v184
	v_readfirstlane_b32 s28, v187
	s_addc_u32 s27, s5, s3
	s_mov_b32 m0, s28
	s_add_u32 s28, s26, 0x10000
	global_load_lds_dwordx4 v2, s[26:27]
	v_mfma_scale_f32_16x16x128_f8f6f4 v[136:139], v[20:27], v[226:233], v[136:139], v186, v185 op_sel_hi:[0,0,0]
	v_mfma_scale_f32_16x16x128_f8f6f4 v[132:135], v[28:35], v[226:233], v[132:135], v186, v185 op_sel_hi:[0,0,0]
	v_mov_b32_e32 v2, v184
	v_readfirstlane_b32 s30, v188
	s_addc_u32 s29, s27, 0
	s_mov_b32 m0, s30
	v_readfirstlane_b32 s30, v189
	global_load_lds_dwordx4 v2, s[28:29]
	v_mfma_scale_f32_16x16x128_f8f6f4 v[128:131], v[20:27], v[234:241], v[128:131], v186, v185 op_sel_hi:[0,0,0]
	v_mfma_scale_f32_16x16x128_f8f6f4 v[124:127], v[28:35], v[234:241], v[124:127], v186, v185 op_sel_hi:[0,0,0]
	s_add_u32 s28, s26, 0x20000
	v_mov_b32_e32 v2, v184
	s_addc_u32 s29, s27, 0
	s_mov_b32 m0, s30
	s_add_u32 s26, s26, 0x30000
	global_load_lds_dwordx4 v2, s[28:29]
	v_mfma_scale_f32_16x16x128_f8f6f4 v[120:123], v[20:27], v[242:249], v[120:123], v186, v185 op_sel_hi:[0,0,0]
	v_mfma_scale_f32_16x16x128_f8f6f4 v[116:119], v[28:35], v[242:249], v[116:119], v186, v185 op_sel_hi:[0,0,0]
	s_setprio 0
	s_setprio 1
	v_mfma_scale_f32_16x16x128_f8f6f4 v[80:83], v[4:11], v[218:225], v[80:83], v186, v185 op_sel_hi:[0,0,0]
	v_mov_b32_e32 v2, v184
	v_readfirstlane_b32 s28, v190
	s_addc_u32 s27, s27, 0
	s_mov_b32 m0, s28
	s_add_u32 s2, s6, s2
	global_load_lds_dwordx4 v2, s[26:27]
	v_mfma_scale_f32_16x16x128_f8f6f4 v[76:79], v[12:19], v[218:225], v[76:79], v186, v185 op_sel_hi:[0,0,0]
	v_mfma_scale_f32_16x16x128_f8f6f4 v[72:75], v[4:11], v[226:233], v[72:75], v186, v185 op_sel_hi:[0,0,0]
	v_mov_b32_e32 v2, v180
	v_readfirstlane_b32 s26, v191
	s_addc_u32 s3, s7, s3
	s_mov_b32 m0, s26
	v_readfirstlane_b32 s26, v201
	global_load_lds_dwordx4 v2, s[2:3]
	v_mfma_scale_f32_16x16x128_f8f6f4 v[68:71], v[12:19], v[226:233], v[68:71], v186, v185 op_sel_hi:[0,0,0]
	v_mfma_scale_f32_16x16x128_f8f6f4 v[64:67], v[4:11], v[234:241], v[64:67], v186, v185 op_sel_hi:[0,0,0]
	v_mov_b32_e32 v2, v181
	s_mov_b32 m0, s26
	s_nop 0
	global_load_lds_dwordx4 v2, s[2:3]
	v_mfma_scale_f32_16x16x128_f8f6f4 v[60:63], v[12:19], v[234:241], v[60:63], v186, v185 op_sel_hi:[0,0,0]
	v_mfma_scale_f32_16x16x128_f8f6f4 v[56:59], v[4:11], v[242:249], v[56:59], v186, v185 op_sel_hi:[0,0,0]
	v_mfma_scale_f32_16x16x128_f8f6f4 v[52:55], v[12:19], v[242:249], v[52:55], v186, v185 op_sel_hi:[0,0,0]
	s_setprio 0
	s_barrier
	ds_read_b128 v[20:23], v212
	ds_read_b128 v[24:27], v212 offset:1024
	ds_read_b128 v[28:31], v212 offset:2048
	ds_read_b128 v[32:35], v212 offset:3072
	ds_read_b128 v[4:7], v213
	ds_read_b128 v[8:11], v213 offset:1024
	ds_read_b128 v[12:15], v213 offset:2048
	ds_read_b128 v[16:19], v213 offset:3072
	ds_read_b128 v[218:221], v214 offset:32768
	ds_read_b128 v[222:225], v214 offset:33792
	ds_read_b128 v[226:229], v215 offset:32768
	ds_read_b128 v[230:233], v215 offset:33792
	ds_read_b128 v[234:237], v216 offset:32768
	ds_read_b128 v[238:241], v216 offset:33792
	ds_read_b128 v[242:245], v217 offset:32768
	ds_read_b128 v[246:249], v217 offset:33792
	s_waitcnt vmcnt(6)
	s_waitcnt lgkmcnt(0)
	s_barrier
	s_setprio 1
	s_waitcnt lgkmcnt(0)
	v_mfma_scale_f32_16x16x128_f8f6f4 v[176:179], v[20:27], v[218:225], v[176:179], v186, v185 op_sel_hi:[0,0,0]
	v_mfma_scale_f32_16x16x128_f8f6f4 v[172:175], v[28:35], v[218:225], v[172:175], v186, v185 op_sel_hi:[0,0,0]
	v_mfma_scale_f32_16x16x128_f8f6f4 v[168:171], v[20:27], v[226:233], v[168:171], v186, v185 op_sel_hi:[0,0,0]
	v_mfma_scale_f32_16x16x128_f8f6f4 v[164:167], v[28:35], v[226:233], v[164:167], v186, v185 op_sel_hi:[0,0,0]
	v_mov_b32_e32 v2, v182
	v_readfirstlane_b32 s26, v202
	s_mov_b32 m0, s26
	v_readfirstlane_b32 s26, v203
	global_load_lds_dwordx4 v2, s[2:3]
	v_mfma_scale_f32_16x16x128_f8f6f4 v[160:163], v[20:27], v[234:241], v[160:163], v186, v185 op_sel_hi:[0,0,0]
	v_mfma_scale_f32_16x16x128_f8f6f4 v[156:159], v[28:35], v[234:241], v[156:159], v186, v185 op_sel_hi:[0,0,0]
	v_mfma_scale_f32_16x16x128_f8f6f4 v[152:155], v[20:27], v[242:249], v[152:155], v186, v185 op_sel_hi:[0,0,0]
	v_mfma_scale_f32_16x16x128_f8f6f4 v[148:151], v[28:35], v[242:249], v[148:151], v186, v185 op_sel_hi:[0,0,0]
	s_setprio 0
	s_setprio 1
	v_mfma_scale_f32_16x16x128_f8f6f4 v[112:115], v[4:11], v[218:225], v[112:115], v186, v185 op_sel_hi:[0,0,0]
	v_mfma_scale_f32_16x16x128_f8f6f4 v[108:111], v[12:19], v[218:225], v[108:111], v186, v185 op_sel_hi:[0,0,0]
	v_mov_b32_e32 v2, v183
	s_mov_b32 m0, s26
	s_nop 0
	global_load_lds_dwordx4 v2, s[2:3]
	v_mfma_scale_f32_16x16x128_f8f6f4 v[104:107], v[4:11], v[226:233], v[104:107], v186, v185 op_sel_hi:[0,0,0]
	v_mfma_scale_f32_16x16x128_f8f6f4 v[100:103], v[12:19], v[226:233], v[100:103], v186, v185 op_sel_hi:[0,0,0]
	v_mfma_scale_f32_16x16x128_f8f6f4 v[96:99], v[4:11], v[234:241], v[96:99], v186, v185 op_sel_hi:[0,0,0]
	v_mfma_scale_f32_16x16x128_f8f6f4 v[92:95], v[12:19], v[234:241], v[92:95], v186, v185 op_sel_hi:[0,0,0]
	v_mfma_scale_f32_16x16x128_f8f6f4 v[88:91], v[4:11], v[242:249], v[88:91], v186, v185 op_sel_hi:[0,0,0]
	v_mfma_scale_f32_16x16x128_f8f6f4 v[84:87], v[12:19], v[242:249], v[84:87], v186, v185 op_sel_hi:[0,0,0]
	s_setprio 0
	s_barrier
	ds_read_b128 v[218:221], v214 offset:49152
	ds_read_b128 v[222:225], v214 offset:50176
	ds_read_b128 v[226:229], v215 offset:49152
	ds_read_b128 v[230:233], v215 offset:50176
	ds_read_b128 v[234:237], v216 offset:49152
	ds_read_b128 v[238:241], v216 offset:50176
	ds_read_b128 v[242:245], v217 offset:49152
	ds_read_b128 v[246:249], v217 offset:50176
	s_waitcnt vmcnt(2)
	s_waitcnt lgkmcnt(0)
	s_barrier
	s_setprio 1
	s_waitcnt lgkmcnt(0)
	v_mfma_scale_f32_16x16x128_f8f6f4 v[144:147], v[20:27], v[218:225], v[144:147], v186, v185 op_sel_hi:[0,0,0]
	v_mfma_scale_f32_16x16x128_f8f6f4 v[140:143], v[28:35], v[218:225], v[140:143], v186, v185 op_sel_hi:[0,0,0]
	s_add_i32 s82, s82, 1
	s_lshl_b64 s[2:3], s[82:83], 7
	s_add_u32 s26, s4, s2
	v_mov_b32_e32 v2, v184
	v_readfirstlane_b32 s28, v204
	s_addc_u32 s27, s5, s3
	s_mov_b32 m0, s28
	s_add_u32 s28, s26, 0x10000
	global_load_lds_dwordx4 v2, s[26:27]
	v_mfma_scale_f32_16x16x128_f8f6f4 v[136:139], v[20:27], v[226:233], v[136:139], v186, v185 op_sel_hi:[0,0,0]
	v_mfma_scale_f32_16x16x128_f8f6f4 v[132:135], v[28:35], v[226:233], v[132:135], v186, v185 op_sel_hi:[0,0,0]
	v_mov_b32_e32 v2, v184
	v_readfirstlane_b32 s30, v205
	s_addc_u32 s29, s27, 0
	s_mov_b32 m0, s30
	v_readfirstlane_b32 s30, v208
	global_load_lds_dwordx4 v2, s[28:29]
	v_mfma_scale_f32_16x16x128_f8f6f4 v[128:131], v[20:27], v[234:241], v[128:131], v186, v185 op_sel_hi:[0,0,0]
	v_mfma_scale_f32_16x16x128_f8f6f4 v[124:127], v[28:35], v[234:241], v[124:127], v186, v185 op_sel_hi:[0,0,0]
	s_add_u32 s28, s26, 0x20000
	v_mov_b32_e32 v2, v184
	s_addc_u32 s29, s27, 0
	s_mov_b32 m0, s30
	s_add_u32 s26, s26, 0x30000
	global_load_lds_dwordx4 v2, s[28:29]
	v_mfma_scale_f32_16x16x128_f8f6f4 v[120:123], v[20:27], v[242:249], v[120:123], v186, v185 op_sel_hi:[0,0,0]
	v_mfma_scale_f32_16x16x128_f8f6f4 v[116:119], v[28:35], v[242:249], v[116:119], v186, v185 op_sel_hi:[0,0,0]
	s_setprio 0
	s_setprio 1
	v_mfma_scale_f32_16x16x128_f8f6f4 v[80:83], v[4:11], v[218:225], v[80:83], v186, v185 op_sel_hi:[0,0,0]
	v_mov_b32_e32 v2, v184
	v_readfirstlane_b32 s28, v209
	s_addc_u32 s27, s27, 0
	s_mov_b32 m0, s28
	s_add_u32 s2, s6, s2
	global_load_lds_dwordx4 v2, s[26:27]
	v_mfma_scale_f32_16x16x128_f8f6f4 v[76:79], v[12:19], v[218:225], v[76:79], v186, v185 op_sel_hi:[0,0,0]
	v_mfma_scale_f32_16x16x128_f8f6f4 v[72:75], v[4:11], v[226:233], v[72:75], v186, v185 op_sel_hi:[0,0,0]
	v_mov_b32_e32 v2, v180
	v_readfirstlane_b32 s26, v206
	s_addc_u32 s3, s7, s3
	s_mov_b32 m0, s26
	v_readfirstlane_b32 s26, v207
	global_load_lds_dwordx4 v2, s[2:3]
	v_mfma_scale_f32_16x16x128_f8f6f4 v[68:71], v[12:19], v[226:233], v[68:71], v186, v185 op_sel_hi:[0,0,0]
	v_mfma_scale_f32_16x16x128_f8f6f4 v[64:67], v[4:11], v[234:241], v[64:67], v186, v185 op_sel_hi:[0,0,0]
	v_mov_b32_e32 v2, v181
	s_mov_b32 m0, s26
	s_nop 0
	global_load_lds_dwordx4 v2, s[2:3]
	v_mfma_scale_f32_16x16x128_f8f6f4 v[60:63], v[12:19], v[234:241], v[60:63], v186, v185 op_sel_hi:[0,0,0]
	v_mfma_scale_f32_16x16x128_f8f6f4 v[56:59], v[4:11], v[242:249], v[56:59], v186, v185 op_sel_hi:[0,0,0]
	v_mfma_scale_f32_16x16x128_f8f6f4 v[52:55], v[12:19], v[242:249], v[52:55], v186, v185 op_sel_hi:[0,0,0]
	s_setprio 0
	s_barrier
	s_add_i32 s25, s25, 2
	s_add_u32 s12, s12, 0x100
	s_addc_u32 s13, s13, 0
	s_cmp_gt_u32 s25, 5
	s_cbranch_scc1 .LBB0_263
.LBB0_259:
	ds_read_b128 v[20:23], v210
	ds_read_b128 v[24:27], v210 offset:1024
	ds_read_b128 v[28:31], v210 offset:2048
	ds_read_b128 v[32:35], v210 offset:3072
	ds_read_b128 v[4:7], v211
	ds_read_b128 v[8:11], v211 offset:1024
	ds_read_b128 v[12:15], v211 offset:2048
	ds_read_b128 v[16:19], v211 offset:3072
	ds_read_b128 v[218:221], v214
	ds_read_b128 v[222:225], v214 offset:1024
	ds_read_b128 v[226:229], v215
	ds_read_b128 v[230:233], v215 offset:1024
	ds_read_b128 v[234:237], v216
	ds_read_b128 v[238:241], v216 offset:1024
	ds_read_b128 v[242:245], v217
	ds_read_b128 v[246:249], v217 offset:1024
	s_waitcnt vmcnt(6)
	s_waitcnt lgkmcnt(0)
	s_barrier
	s_setprio 1
	s_waitcnt lgkmcnt(0)
	v_mfma_scale_f32_16x16x128_f8f6f4 v[176:179], v[20:27], v[218:225], v[176:179], v186, v185 op_sel_hi:[0,0,0]
	v_mfma_scale_f32_16x16x128_f8f6f4 v[172:175], v[28:35], v[218:225], v[172:175], v186, v185 op_sel_hi:[0,0,0]
	v_mfma_scale_f32_16x16x128_f8f6f4 v[168:171], v[20:27], v[226:233], v[168:171], v186, v185 op_sel_hi:[0,0,0]
	v_mfma_scale_f32_16x16x128_f8f6f4 v[164:167], v[28:35], v[226:233], v[164:167], v186, v185 op_sel_hi:[0,0,0]
	s_add_u32 s2, s6, s12
	s_addc_u32 s3, s7, s13
	v_add_u32_e32 v192, 0xc000, v191
	s_add_u32 s2, s2, 0x80
	v_mov_b32_e32 v2, v182
	v_readfirstlane_b32 s26, v192
	v_add_u32_e32 v192, 0xe000, v191
	s_addc_u32 s3, s3, 0
	s_mov_b32 m0, s26
	v_readfirstlane_b32 s26, v192
	global_load_lds_dwordx4 v2, s[2:3]
	v_mfma_scale_f32_16x16x128_f8f6f4 v[160:163], v[20:27], v[234:241], v[160:163], v186, v185 op_sel_hi:[0,0,0]
	v_mfma_scale_f32_16x16x128_f8f6f4 v[156:159], v[28:35], v[234:241], v[156:159], v186, v185 op_sel_hi:[0,0,0]
	v_mfma_scale_f32_16x16x128_f8f6f4 v[152:155], v[20:27], v[242:249], v[152:155], v186, v185 op_sel_hi:[0,0,0]
	v_mfma_scale_f32_16x16x128_f8f6f4 v[148:151], v[28:35], v[242:249], v[148:151], v186, v185 op_sel_hi:[0,0,0]
	s_setprio 0
	s_setprio 1
	v_mfma_scale_f32_16x16x128_f8f6f4 v[112:115], v[4:11], v[218:225], v[112:115], v186, v185 op_sel_hi:[0,0,0]
	v_mfma_scale_f32_16x16x128_f8f6f4 v[108:111], v[12:19], v[218:225], v[108:111], v186, v185 op_sel_hi:[0,0,0]
	v_mov_b32_e32 v2, v183
	s_mov_b32 m0, s26
	s_nop 0
	global_load_lds_dwordx4 v2, s[2:3]
	v_mfma_scale_f32_16x16x128_f8f6f4 v[104:107], v[4:11], v[226:233], v[104:107], v186, v185 op_sel_hi:[0,0,0]
	v_mfma_scale_f32_16x16x128_f8f6f4 v[100:103], v[12:19], v[226:233], v[100:103], v186, v185 op_sel_hi:[0,0,0]
	v_mfma_scale_f32_16x16x128_f8f6f4 v[96:99], v[4:11], v[234:241], v[96:99], v186, v185 op_sel_hi:[0,0,0]
	v_mfma_scale_f32_16x16x128_f8f6f4 v[92:95], v[12:19], v[234:241], v[92:95], v186, v185 op_sel_hi:[0,0,0]
	v_mfma_scale_f32_16x16x128_f8f6f4 v[88:91], v[4:11], v[242:249], v[88:91], v186, v185 op_sel_hi:[0,0,0]
	v_mfma_scale_f32_16x16x128_f8f6f4 v[84:87], v[12:19], v[242:249], v[84:87], v186, v185 op_sel_hi:[0,0,0]
	s_cmp_lg_u32 s25, 4
	s_setprio 0
	s_barrier
	s_cbranch_scc1 .LBB0_262
	s_cmpk_gt_u32 s15, 0xd7f
	s_mov_b64 s[20:21], 0
	s_cbranch_scc1 .LBB0_257
	s_load_dword s2, s[64:65], 0x10
	s_load_dword s4, s[64:65], 0x0
	v_mov_b32_e32 v2, v0
	s_mov_b64 s[20:21], -1
	v_ashrrev_i32_e32 v181, 31, v2
	v_lshrrev_b32_e32 v181, 26, v181
	v_lshlrev_b32_e32 v180, 4, v2
	v_add_u32_e32 v181, v2, v181
	v_bfe_i32 v2, v2, 27, 1
	s_waitcnt lgkmcnt(0)
	s_lshr_b32 s2, s2, 16
	v_lshrrev_b32_e32 v2, 22, v2
	s_cmp_lg_u32 s2, 0
	v_add_u32_e32 v2, v180, v2
	s_cselect_b64 s[2:3], -1, 0
	v_and_b32_e32 v2, 0xfffffc00, v2
	s_cmp_lg_u64 s[2:3], 0
	v_sub_u32_e32 v2, v180, v2
	s_addc_u32 s16, s4, s15
	s_lshr_b32 s3, s15, 3
	v_lshrrev_b32_e32 v180, 4, v2
	s_and_b32 s2, s15, 7
	s_add_i32 s4, s3, 0xffffff28
	v_bitop3_b32 v2, v180, v2, 32 bitop3:0x6c
	s_cmpk_lt_u32 s15, 0x6c0
	v_ashrrev_i32_e32 v182, 31, v2
	s_cselect_b32 s3, s3, s4
	s_cmpk_gt_u32 s15, 0x6bf
	v_lshrrev_b32_e32 v182, 26, v182
	s_cselect_b32 s4, 8, 0
	s_and_b32 s5, s3, 7
	v_add_u32_e32 v182, v2, v182
	s_or_b32 s4, s5, s4
	v_lshrrev_b32_e32 v183, 6, v182
	v_and_b32_e32 v182, 0xc0, v182
	s_lshr_b32 s82, s3, 3
	s_lshl_b32 s3, s4, 3
	v_ashrrev_i32_e32 v181, 6, v181
	v_sub_u32_e32 v2, v2, v182
	s_or_b32 s14, s3, s2
	v_lshlrev_b32_e32 v180, 3, v181
	v_lshlrev_b32_e32 v181, 5, v181
	v_ashrrev_i16_sdwa v2, v196, sext(v2) dst_sel:DWORD dst_unused:UNUSED_PAD src0_sel:DWORD src1_sel:BYTE_0
	s_lshl_b64 s[2:3], s[82:83], 18
	v_and_b32_e32 v180, 0x3ffff0, v180
	v_and_b32_e32 v181, 32, v181
	v_bfe_i32 v2, v2, 0, 16
	s_add_u32 s4, s19, s2
	s_addc_u32 s5, s22, s3
	s_lshl_b32 s2, s14, 18
	v_add_lshl_u32 v180, v183, v180, 10
	v_add_lshl_u32 v2, v181, v2, 1
	v_add3_u32 v180, v180, s2, v2
	v_add_u32_e32 v181, 0x10000, v180
	v_add_u32_e32 v182, 0x20000, v180
	v_add_u32_e32 v183, 0x30000, v180
	s_mov_b64 s[6:7], s[8:9]
	s_mov_b32 s15, s16
	s_mov_b32 s16, s82
	s_branch .LBB0_257
